# speedup vs baseline: 1.0117x; 1.0117x over previous
.LBB1_1:
	ds_read_b128 v[212:215], v242 offset:0
	ds_read_b128 v[216:219], v242 offset:0x800
	ds_read_b128 v[220:223], v242 offset:0x1000
	ds_read_b128 v[224:227], v242 offset:0x1800
	ds_read_b128 v[228:231], v211 offset:0
	ds_read_b128 v[232:235], v211 offset:0x800
	ds_read_b128 v[236:239], v211 offset:0x1000
	s_waitcnt lgkmcnt(2)
	v_mfma_f32_16x16x32_bf16 v[174:177], v[212:215], v[228:231], v[174:177]
	v_mfma_f32_16x16x32_bf16 v[170:173], v[216:219], v[228:231], v[170:173]
	v_mfma_f32_16x16x32_bf16 v[166:169], v[220:223], v[228:231], v[166:169]
	v_mfma_f32_16x16x32_bf16 v[162:165], v[224:227], v[228:231], v[162:165]
	ds_read_b128 v[228:231], v211 offset:0x1800
	s_waitcnt lgkmcnt(2)
	v_mfma_f32_16x16x32_bf16 v[158:161], v[212:215], v[232:235], v[158:161]
	v_mfma_f32_16x16x32_bf16 v[154:157], v[216:219], v[232:235], v[154:157]
	v_mfma_f32_16x16x32_bf16 v[150:153], v[220:223], v[232:235], v[150:153]
	v_mfma_f32_16x16x32_bf16 v[146:149], v[224:227], v[232:235], v[146:149]
	ds_read_b128 v[232:235], v211 offset:0x2000
	s_waitcnt lgkmcnt(2)
	v_mfma_f32_16x16x32_bf16 v[142:145], v[212:215], v[236:239], v[142:145]
	v_mfma_f32_16x16x32_bf16 v[138:141], v[216:219], v[236:239], v[138:141]
	v_mfma_f32_16x16x32_bf16 v[134:137], v[220:223], v[236:239], v[134:137]
	v_mfma_f32_16x16x32_bf16 v[130:133], v[224:227], v[236:239], v[130:133]
	ds_read_b128 v[236:239], v211 offset:0x2800
	s_waitcnt lgkmcnt(2)
	v_mfma_f32_16x16x32_bf16 v[126:129], v[212:215], v[228:231], v[126:129]
	v_mfma_f32_16x16x32_bf16 v[122:125], v[216:219], v[228:231], v[122:125]
	v_mfma_f32_16x16x32_bf16 v[118:121], v[220:223], v[228:231], v[118:121]
	v_mfma_f32_16x16x32_bf16 v[114:117], v[224:227], v[228:231], v[114:117]
	ds_read_b128 v[228:231], v211 offset:0x3000
	s_waitcnt lgkmcnt(2)
	v_mfma_f32_16x16x32_bf16 v[110:113], v[212:215], v[232:235], v[110:113]
	v_mfma_f32_16x16x32_bf16 v[106:109], v[216:219], v[232:235], v[106:109]
	v_mfma_f32_16x16x32_bf16 v[102:105], v[220:223], v[232:235], v[102:105]
	v_mfma_f32_16x16x32_bf16 v[98:101], v[224:227], v[232:235], v[98:101]
	ds_read_b128 v[232:235], v211 offset:0x3800
	s_waitcnt lgkmcnt(2)
	v_mfma_f32_16x16x32_bf16 v[94:97], v[212:215], v[236:239], v[94:97]
	v_mfma_f32_16x16x32_bf16 v[90:93], v[216:219], v[236:239], v[90:93]
	v_mfma_f32_16x16x32_bf16 v[86:89], v[220:223], v[236:239], v[86:89]
	v_mfma_f32_16x16x32_bf16 v[82:85], v[224:227], v[236:239], v[82:85]
	s_waitcnt lgkmcnt(1)
	v_mfma_f32_16x16x32_bf16 v[78:81], v[212:215], v[228:231], v[78:81]
	v_mfma_f32_16x16x32_bf16 v[74:77], v[216:219], v[228:231], v[74:77]
	v_mfma_f32_16x16x32_bf16 v[70:73], v[220:223], v[228:231], v[70:73]
	v_mfma_f32_16x16x32_bf16 v[66:69], v[224:227], v[228:231], v[66:69]
	s_waitcnt lgkmcnt(0)
	v_mfma_f32_16x16x32_bf16 v[62:65], v[212:215], v[232:235], v[62:65]
	v_mfma_f32_16x16x32_bf16 v[58:61], v[216:219], v[232:235], v[58:61]
	v_mfma_f32_16x16x32_bf16 v[54:57], v[220:223], v[232:235], v[54:57]
	v_mfma_f32_16x16x32_bf16 v[50:53], v[224:227], v[232:235], v[50:53]
	s_xor_b32 s0, s0, 0x10000
	s_and_b32 s1, s22, 0x3c0
	s_add_i32 s23, s0, 0
	s_lshl_b32 s0, s1, 2
	s_add_u32 s20, s25, s0
	s_waitcnt vmcnt(10)
	v_cvt_pk_bf16_f32 v46, v46, v47
	v_cvt_pk_bf16_f32 v47, v48, v49
	v_cvt_pk_bf16_f32 v48, v42, v43
	v_cvt_pk_bf16_f32 v49, v44, v45
	s_waitcnt vmcnt(8)
	v_cvt_pk_bf16_f32 v38, v38, v39
	v_cvt_pk_bf16_f32 v39, v40, v41
	v_cvt_pk_bf16_f32 v40, v34, v35
	v_add_u32_e32 v34, s23, v208
	s_addc_u32 s21, s26, 0
	s_lshl_b32 s0, s1, 1
	v_cvt_pk_bf16_f32 v41, v36, v37
	v_lshlrev_b32_e32 v182, 2, v178
	v_add_u32_e32 v35, s23, v205
	v_add_u32_e32 v36, s23, v206
	v_add_u32_e32 v37, s23, v207
	ds_write_b128 v34, v[46:49]
	ds_write_b128 v35, v[38:41]
	s_waitcnt vmcnt(7)
	ds_write_b128 v36, v[30:33] offset:32768
	s_waitcnt vmcnt(6)
	ds_write_b128 v37, v[26:29] offset:32768
	v_lshl_add_u64 v[26:27], s[20:21], 0, v[180:181]
	v_lshl_add_u64 v[28:29], s[20:21], 0, v[184:185]
	s_add_u32 s0, s27, s0
	v_lshl_add_u64 v[26:27], v[26:27], 0, v[182:183]
	v_lshl_add_u64 v[28:29], v[28:29], 0, v[182:183]
	s_addc_u32 s1, s28, 0
	v_lshlrev_b32_e32 v240, 1, v178
	v_mov_b32_e32 v241, v183
	global_load_dwordx4 v[42:45], v[26:27], off offset:16
	global_load_dwordx4 v[46:49], v[26:27], off
	global_load_dwordx4 v[34:37], v[28:29], off offset:16
	global_load_dwordx4 v[38:41], v[28:29], off
	v_lshl_add_u64 v[26:27], s[0:1], 0, v[186:187]
	v_lshl_add_u64 v[28:29], s[0:1], 0, v[188:189]
	v_lshl_add_u64 v[26:27], v[26:27], 0, v[240:241]
	v_lshl_add_u64 v[28:29], v[28:29], 0, v[240:241]
	global_load_dwordx4 v[30:33], v[26:27], off
	s_nop 0
	global_load_dwordx4 v[26:29], v[28:29], off
	ds_read_b128 v[212:215], v242 offset:0x400
	ds_read_b128 v[216:219], v242 offset:0xc00
	ds_read_b128 v[220:223], v242 offset:0x1400
	ds_read_b128 v[224:227], v242 offset:0x1c00
	ds_read_b128 v[228:231], v211 offset:0x400
	ds_read_b128 v[232:235], v211 offset:0xc00
	ds_read_b128 v[236:239], v211 offset:0x1400
	s_waitcnt lgkmcnt(2)
	v_mfma_f32_16x16x32_bf16 v[174:177], v[212:215], v[228:231], v[174:177]
	v_mfma_f32_16x16x32_bf16 v[170:173], v[216:219], v[228:231], v[170:173]
	v_mfma_f32_16x16x32_bf16 v[166:169], v[220:223], v[228:231], v[166:169]
	v_mfma_f32_16x16x32_bf16 v[162:165], v[224:227], v[228:231], v[162:165]
	ds_read_b128 v[228:231], v211 offset:0x1c00
	s_waitcnt lgkmcnt(2)
	v_mfma_f32_16x16x32_bf16 v[158:161], v[212:215], v[232:235], v[158:161]
	v_mfma_f32_16x16x32_bf16 v[154:157], v[216:219], v[232:235], v[154:157]
	v_mfma_f32_16x16x32_bf16 v[150:153], v[220:223], v[232:235], v[150:153]
	v_mfma_f32_16x16x32_bf16 v[146:149], v[224:227], v[232:235], v[146:149]
	ds_read_b128 v[232:235], v211 offset:0x2400
	s_waitcnt lgkmcnt(2)
	v_mfma_f32_16x16x32_bf16 v[142:145], v[212:215], v[236:239], v[142:145]
	v_mfma_f32_16x16x32_bf16 v[138:141], v[216:219], v[236:239], v[138:141]
	v_mfma_f32_16x16x32_bf16 v[134:137], v[220:223], v[236:239], v[134:137]
	v_mfma_f32_16x16x32_bf16 v[130:133], v[224:227], v[236:239], v[130:133]
	ds_read_b128 v[236:239], v211 offset:0x2c00
	s_waitcnt lgkmcnt(2)
	v_mfma_f32_16x16x32_bf16 v[126:129], v[212:215], v[228:231], v[126:129]
	v_mfma_f32_16x16x32_bf16 v[122:125], v[216:219], v[228:231], v[122:125]
	v_mfma_f32_16x16x32_bf16 v[118:121], v[220:223], v[228:231], v[118:121]
	v_mfma_f32_16x16x32_bf16 v[114:117], v[224:227], v[228:231], v[114:117]
	ds_read_b128 v[228:231], v211 offset:0x3400
	s_waitcnt lgkmcnt(2)
	v_mfma_f32_16x16x32_bf16 v[110:113], v[212:215], v[232:235], v[110:113]
	v_mfma_f32_16x16x32_bf16 v[106:109], v[216:219], v[232:235], v[106:109]
	v_mfma_f32_16x16x32_bf16 v[102:105], v[220:223], v[232:235], v[102:105]
	v_mfma_f32_16x16x32_bf16 v[98:101], v[224:227], v[232:235], v[98:101]
	ds_read_b128 v[232:235], v211 offset:0x3c00
	s_waitcnt lgkmcnt(2)
	v_mfma_f32_16x16x32_bf16 v[94:97], v[212:215], v[236:239], v[94:97]
	v_mfma_f32_16x16x32_bf16 v[90:93], v[216:219], v[236:239], v[90:93]
	v_mfma_f32_16x16x32_bf16 v[86:89], v[220:223], v[236:239], v[86:89]
	v_mfma_f32_16x16x32_bf16 v[82:85], v[224:227], v[236:239], v[82:85]
	s_waitcnt lgkmcnt(1)
	v_mfma_f32_16x16x32_bf16 v[78:81], v[212:215], v[228:231], v[78:81]
	v_mfma_f32_16x16x32_bf16 v[74:77], v[216:219], v[228:231], v[74:77]
	v_mfma_f32_16x16x32_bf16 v[70:73], v[220:223], v[228:231], v[70:73]
	v_mfma_f32_16x16x32_bf16 v[66:69], v[224:227], v[228:231], v[66:69]
	s_waitcnt lgkmcnt(0)
	v_mfma_f32_16x16x32_bf16 v[62:65], v[212:215], v[232:235], v[62:65]
	v_mfma_f32_16x16x32_bf16 v[58:61], v[216:219], v[232:235], v[58:61]
	v_mfma_f32_16x16x32_bf16 v[54:57], v[220:223], v[232:235], v[54:57]
	v_mfma_f32_16x16x32_bf16 v[50:53], v[224:227], v[232:235], v[50:53]
	s_waitcnt vmcnt(10)
	v_cvt_pk_bf16_f32 v22, v22, v23
	v_cvt_pk_bf16_f32 v23, v24, v25
	v_cvt_pk_bf16_f32 v24, v6, v7
	v_cvt_pk_bf16_f32 v25, v8, v9
	v_add_u32_e32 v6, s23, v204
	s_waitcnt vmcnt(9)
	v_cvt_pk_bf16_f32 v8, v2, v3
	v_add_u32_e32 v2, s23, v201
	ds_write_b128 v6, v[22:25]
	s_waitcnt vmcnt(8)
	v_cvt_pk_bf16_f32 v6, v10, v11
	v_cvt_pk_bf16_f32 v7, v12, v13
	v_cvt_pk_bf16_f32 v9, v4, v5
	ds_write_b128 v2, v[6:9]
	v_add_u32_e32 v2, s23, v202
	s_waitcnt vmcnt(7)
	ds_write_b128 v2, v[18:21] offset:32768
	v_add_u32_e32 v2, s23, v203
	s_waitcnt vmcnt(6)
	ds_write_b128 v2, v[14:17] offset:32768
	v_lshl_add_u64 v[2:3], s[20:21], 0, v[190:191]
	v_lshl_add_u64 v[2:3], v[2:3], 0, v[182:183]
	global_load_dwordx4 v[6:9], v[2:3], off offset:16
	global_load_dwordx4 v[22:25], v[2:3], off
	v_lshl_add_u64 v[2:3], s[20:21], 0, v[192:193]
	v_lshl_add_u64 v[14:15], s[0:1], 0, v[194:195]
	v_lshl_add_u64 v[16:17], s[0:1], 0, v[196:197]
	v_lshl_add_u64 v[10:11], v[2:3], 0, v[182:183]
	v_lshl_add_u64 v[14:15], v[14:15], 0, v[240:241]
	v_lshl_add_u64 v[16:17], v[16:17], 0, v[240:241]
	global_load_dwordx4 v[2:5], v[10:11], off offset:16
	s_nop 0
	global_load_dwordx4 v[10:13], v[10:11], off
	s_nop 0
	global_load_dwordx4 v[18:21], v[14:15], off
	s_nop 0
	global_load_dwordx4 v[14:17], v[16:17], off
	s_waitcnt lgkmcnt(0)
	s_add_i32 s22, s22, 64
	s_add_i32 s29, s29, 0x10000
	s_and_b32 s0, s29, 0x10000
	v_add_u32_e32 v211, s0, v209
	v_add_u32_e32 v242, s0, v210
	s_cmp_lg_u32 s29, 0xe0000
	s_barrier
	s_cbranch_scc1 .LBB1_1
	s_lshl_b64 s[0:1], s[18:19], 24
	ds_read_b128 v[180:183], v210 offset:0
	ds_read_b128 v[184:187], v210 offset:0x800
	ds_read_b128 v[188:191], v210 offset:0x1000
	ds_read_b128 v[192:195], v210 offset:0x1800
	ds_read_b128 v[212:215], v209 offset:0
	ds_read_b128 v[216:219], v209 offset:0x800
	ds_read_b128 v[220:223], v209 offset:0x1000
	s_waitcnt lgkmcnt(0)
	s_add_u32 s0, s10, s0
	s_addc_u32 s18, s11, s1
	s_lshl_b32 s19, s24, 1
	s_mov_b32 s1, 0
	s_add_u32 s0, s0, s19
	s_waitcnt lgkmcnt(2)
	s_addc_u32 s20, s18, 0
	v_mfma_f32_16x16x32_bf16 v[174:177], v[180:183], v[212:215], v[174:177]
	v_mfma_f32_16x16x32_bf16 v[170:173], v[184:187], v[212:215], v[170:173]
	v_mfma_f32_16x16x32_bf16 v[166:169], v[188:191], v[212:215], v[166:169]
	v_mfma_f32_16x16x32_bf16 v[162:165], v[192:195], v[212:215], v[162:165]
	ds_read_b128 v[212:215], v209 offset:0x1800
	s_waitcnt lgkmcnt(2)
	s_nop 0
	v_mfma_f32_16x16x32_bf16 v[158:161], v[180:183], v[216:219], v[158:161]
	v_mfma_f32_16x16x32_bf16 v[154:157], v[184:187], v[216:219], v[154:157]
	v_mfma_f32_16x16x32_bf16 v[150:153], v[188:191], v[216:219], v[150:153]
	v_mfma_f32_16x16x32_bf16 v[146:149], v[192:195], v[216:219], v[146:149]
	ds_read_b128 v[216:219], v209 offset:0x2000
	s_waitcnt lgkmcnt(2)
	s_nop 0
	v_mfma_f32_16x16x32_bf16 v[142:145], v[180:183], v[220:223], v[142:145]
	v_mfma_f32_16x16x32_bf16 v[138:141], v[184:187], v[220:223], v[138:141]
	v_mfma_f32_16x16x32_bf16 v[134:137], v[188:191], v[220:223], v[134:137]
	v_mfma_f32_16x16x32_bf16 v[130:133], v[192:195], v[220:223], v[130:133]
	ds_read_b128 v[220:223], v209 offset:0x2800
	s_waitcnt lgkmcnt(2)
	s_nop 0
	v_mfma_f32_16x16x32_bf16 v[126:129], v[180:183], v[212:215], v[126:129]
	v_mfma_f32_16x16x32_bf16 v[122:125], v[184:187], v[212:215], v[122:125]
	v_mfma_f32_16x16x32_bf16 v[118:121], v[188:191], v[212:215], v[118:121]
	v_mfma_f32_16x16x32_bf16 v[114:117], v[192:195], v[212:215], v[114:117]
	ds_read_b128 v[212:215], v209 offset:0x3000
	s_waitcnt lgkmcnt(2)
	s_nop 0
	v_mfma_f32_16x16x32_bf16 v[110:113], v[180:183], v[216:219], v[110:113]
	v_mfma_f32_16x16x32_bf16 v[106:109], v[184:187], v[216:219], v[106:109]
	v_mfma_f32_16x16x32_bf16 v[102:105], v[188:191], v[216:219], v[102:105]
	v_mfma_f32_16x16x32_bf16 v[98:101], v[192:195], v[216:219], v[98:101]
	ds_read_b128 v[216:219], v209 offset:0x3800
	s_waitcnt lgkmcnt(2)
	s_nop 0
	v_mfma_f32_16x16x32_bf16 v[94:97], v[180:183], v[220:223], v[94:97]
	v_mfma_f32_16x16x32_bf16 v[90:93], v[184:187], v[220:223], v[90:93]
	v_mfma_f32_16x16x32_bf16 v[86:89], v[188:191], v[220:223], v[86:89]
	v_mfma_f32_16x16x32_bf16 v[82:85], v[192:195], v[220:223], v[82:85]
	s_waitcnt lgkmcnt(1)
	s_nop 0
	v_mfma_f32_16x16x32_bf16 v[78:81], v[180:183], v[212:215], v[78:81]
	v_mfma_f32_16x16x32_bf16 v[74:77], v[184:187], v[212:215], v[74:77]
	v_mfma_f32_16x16x32_bf16 v[70:73], v[188:191], v[212:215], v[70:73]
	v_mfma_f32_16x16x32_bf16 v[66:69], v[192:195], v[212:215], v[66:69]
	s_waitcnt lgkmcnt(0)
	s_nop 0
	v_mfma_f32_16x16x32_bf16 v[62:65], v[180:183], v[216:219], v[62:65]
	v_mfma_f32_16x16x32_bf16 v[58:61], v[184:187], v[216:219], v[58:61]
	v_mfma_f32_16x16x32_bf16 v[54:57], v[188:191], v[216:219], v[54:57]
	v_mfma_f32_16x16x32_bf16 v[50:53], v[192:195], v[216:219], v[50:53]
	s_add_i32 s18, 0, 0x10000
	s_waitcnt vmcnt(10)
	v_cvt_pk_bf16_f32 v46, v46, v47
	v_cvt_pk_bf16_f32 v47, v48, v49
	v_cvt_pk_bf16_f32 v48, v42, v43
	v_add_u32_e32 v42, s18, v208
	s_waitcnt vmcnt(8)
	v_cvt_pk_bf16_f32 v38, v38, v39
	v_cvt_pk_bf16_f32 v39, v40, v41
	v_cvt_pk_bf16_f32 v40, v34, v35
	v_add_u32_e32 v34, s18, v205
	s_add_i32 s19, 0, 0x18000
	v_cvt_pk_bf16_f32 v49, v44, v45
	ds_write_b128 v42, v[46:49]
	v_cvt_pk_bf16_f32 v41, v36, v37
	ds_write_b128 v34, v[38:41]
	v_add_u32_e32 v34, s19, v206
	s_waitcnt vmcnt(7)
	ds_write_b128 v34, v[30:33]
	v_add_u32_e32 v30, s19, v207
	s_waitcnt vmcnt(6)
	ds_write_b128 v30, v[26:29]
	ds_read_b128 v[26:29], v210 offset:0x400
	ds_read_b128 v[30:33], v210 offset:0xc00
	ds_read_b128 v[34:37], v210 offset:0x1400
	ds_read_b128 v[38:41], v210 offset:0x1c00
	ds_read_b128 v[42:45], v209 offset:0x400
	ds_read_b128 v[46:49], v209 offset:0xc00
	ds_read_b128 v[180:183], v209 offset:0x1400
	s_nop 0
	s_waitcnt lgkmcnt(2)
	s_nop 0
	v_mfma_f32_16x16x32_bf16 v[174:177], v[26:29], v[42:45], v[174:177]
	v_mfma_f32_16x16x32_bf16 v[170:173], v[30:33], v[42:45], v[170:173]
	v_mfma_f32_16x16x32_bf16 v[166:169], v[34:37], v[42:45], v[166:169]
	v_mfma_f32_16x16x32_bf16 v[42:45], v[38:41], v[42:45], v[162:165]
	ds_read_b128 v[162:165], v209 offset:0x1c00
	s_waitcnt lgkmcnt(2)
	s_nop 0
	v_mfma_f32_16x16x32_bf16 v[158:161], v[26:29], v[46:49], v[158:161]
	v_mfma_f32_16x16x32_bf16 v[154:157], v[30:33], v[46:49], v[154:157]
	v_mfma_f32_16x16x32_bf16 v[150:153], v[34:37], v[46:49], v[150:153]
	v_mfma_f32_16x16x32_bf16 v[46:49], v[38:41], v[46:49], v[146:149]
	ds_read_b128 v[146:149], v209 offset:0x2400
	s_waitcnt lgkmcnt(2)
	s_nop 0
	v_mfma_f32_16x16x32_bf16 v[142:145], v[26:29], v[180:183], v[142:145]
	v_mfma_f32_16x16x32_bf16 v[138:141], v[30:33], v[180:183], v[138:141]
	v_mfma_f32_16x16x32_bf16 v[134:137], v[34:37], v[180:183], v[134:137]
	v_mfma_f32_16x16x32_bf16 v[130:133], v[38:41], v[180:183], v[130:133]
	ds_read_b128 v[180:183], v209 offset:0x2c00
	s_waitcnt lgkmcnt(2)
	s_nop 0
	v_mfma_f32_16x16x32_bf16 v[126:129], v[26:29], v[162:165], v[126:129]
	v_mfma_f32_16x16x32_bf16 v[122:125], v[30:33], v[162:165], v[122:125]
	v_mfma_f32_16x16x32_bf16 v[118:121], v[34:37], v[162:165], v[118:121]
	v_mfma_f32_16x16x32_bf16 v[114:117], v[38:41], v[162:165], v[114:117]
	ds_read_b128 v[162:165], v209 offset:0x3400
	s_waitcnt lgkmcnt(2)
	s_nop 0
	v_mfma_f32_16x16x32_bf16 v[110:113], v[26:29], v[146:149], v[110:113]
	v_mfma_f32_16x16x32_bf16 v[106:109], v[30:33], v[146:149], v[106:109]
	v_mfma_f32_16x16x32_bf16 v[102:105], v[34:37], v[146:149], v[102:105]
	v_mfma_f32_16x16x32_bf16 v[98:101], v[38:41], v[146:149], v[98:101]
	ds_read_b128 v[146:149], v209 offset:0x3c00
	s_waitcnt lgkmcnt(2)
	s_nop 0
	v_mfma_f32_16x16x32_bf16 v[94:97], v[26:29], v[180:183], v[94:97]
	v_mfma_f32_16x16x32_bf16 v[90:93], v[30:33], v[180:183], v[90:93]
	v_mfma_f32_16x16x32_bf16 v[86:89], v[34:37], v[180:183], v[86:89]
	v_mfma_f32_16x16x32_bf16 v[82:85], v[38:41], v[180:183], v[82:85]
	s_waitcnt lgkmcnt(1)
	s_nop 0
	v_mfma_f32_16x16x32_bf16 v[78:81], v[26:29], v[162:165], v[78:81]
	v_mfma_f32_16x16x32_bf16 v[74:77], v[30:33], v[162:165], v[74:77]
	v_mfma_f32_16x16x32_bf16 v[70:73], v[34:37], v[162:165], v[70:73]
	v_mfma_f32_16x16x32_bf16 v[66:69], v[38:41], v[162:165], v[66:69]
	s_waitcnt lgkmcnt(0)
	s_nop 0
	v_mfma_f32_16x16x32_bf16 v[26:29], v[26:29], v[146:149], v[62:65]
	v_mfma_f32_16x16x32_bf16 v[30:33], v[30:33], v[146:149], v[58:61]
	v_mfma_f32_16x16x32_bf16 v[34:37], v[34:37], v[146:149], v[54:57]
	v_mfma_f32_16x16x32_bf16 v[38:41], v[38:41], v[146:149], v[50:53]
	s_waitcnt vmcnt(4)
	v_cvt_pk_bf16_f32 v22, v22, v23
	v_cvt_pk_bf16_f32 v23, v24, v25
	v_cvt_pk_bf16_f32 v24, v6, v7
	v_cvt_pk_bf16_f32 v25, v8, v9
	v_add_u32_e32 v6, s18, v204
	s_waitcnt vmcnt(3)
	v_cvt_pk_bf16_f32 v8, v2, v3
	v_add_u32_e32 v2, s18, v201
	ds_write_b128 v6, v[22:25]
	s_waitcnt vmcnt(2)
	v_cvt_pk_bf16_f32 v6, v10, v11
	v_cvt_pk_bf16_f32 v7, v12, v13
	v_cvt_pk_bf16_f32 v9, v4, v5
	ds_write_b128 v2, v[6:9]
	v_add_u32_e32 v2, s19, v202
	s_waitcnt vmcnt(1)
	ds_write_b128 v2, v[18:21]
	v_add_u32_e32 v2, s19, v203
	s_waitcnt vmcnt(0)
	ds_write_b128 v2, v[14:17]
	s_waitcnt lgkmcnt(0)
	s_barrier
	v_add_u32_e32 v178, 0x10000, v209
	v_add_u32_e32 v196, 0x10000, v210
	ds_read_b128 v[2:5], v196 offset:0
	ds_read_b128 v[6:9], v196 offset:0x800
	ds_read_b128 v[10:13], v196 offset:0x1000
	ds_read_b128 v[14:17], v196 offset:0x1800
	ds_read_b128 v[18:21], v178 offset:0
	s_and_b64 s[16:17], s[16:17], exec
	ds_read_b128 v[22:25], v178 offset:0x800
	ds_read_b128 v[50:53], v178 offset:0x1000
	s_waitcnt lgkmcnt(2)
	s_cselect_b32 s5, s5, s7
	s_cselect_b32 s4, s4, s6
	s_lshl_b32 s6, s3, 10
	v_mfma_f32_16x16x32_bf16 v[54:57], v[2:5], v[18:21], v[174:177]
	s_add_u32 s6, s4, s6
	s_addc_u32 s7, s5, 0
	s_lshl_b32 s3, s3, 9
	v_mfma_f32_16x16x32_bf16 v[58:61], v[6:9], v[18:21], v[170:173]
	s_add_u32 s4, s0, s3
	s_addc_u32 s5, s20, 0
	v_mfma_f32_16x16x32_bf16 v[62:65], v[10:13], v[18:21], v[166:169]
	v_mfma_f32_16x16x32_bf16 v[18:21], v[14:17], v[18:21], v[42:45]
	ds_read_b128 v[42:45], v178 offset:0x1800
	s_waitcnt lgkmcnt(2)
	s_nop 0
	v_mfma_f32_16x16x32_bf16 v[146:149], v[2:5], v[22:25], v[158:161]
	v_mfma_f32_16x16x32_bf16 v[154:157], v[6:9], v[22:25], v[154:157]
	v_mfma_f32_16x16x32_bf16 v[150:153], v[10:13], v[22:25], v[150:153]
	v_mfma_f32_16x16x32_bf16 v[22:25], v[14:17], v[22:25], v[46:49]
	ds_read_b128 v[46:49], v178 offset:0x2000
	s_waitcnt lgkmcnt(2)
	s_nop 0
	v_mfma_f32_16x16x32_bf16 v[142:145], v[2:5], v[50:53], v[142:145]
	v_mfma_f32_16x16x32_bf16 v[138:141], v[6:9], v[50:53], v[138:141]
	v_mfma_f32_16x16x32_bf16 v[134:137], v[10:13], v[50:53], v[134:137]
	v_mfma_f32_16x16x32_bf16 v[50:53], v[14:17], v[50:53], v[130:133]
	ds_read_b128 v[130:133], v178 offset:0x2800
	s_waitcnt lgkmcnt(2)
	s_nop 0
	v_mfma_f32_16x16x32_bf16 v[126:129], v[2:5], v[42:45], v[126:129]
	v_mfma_f32_16x16x32_bf16 v[122:125], v[6:9], v[42:45], v[122:125]
	v_mfma_f32_16x16x32_bf16 v[118:121], v[10:13], v[42:45], v[118:121]
	v_mfma_f32_16x16x32_bf16 v[42:45], v[14:17], v[42:45], v[114:117]
	ds_read_b128 v[114:117], v178 offset:0x3000
	s_waitcnt lgkmcnt(2)
	s_nop 0
	v_mfma_f32_16x16x32_bf16 v[110:113], v[2:5], v[46:49], v[110:113]
	v_mfma_f32_16x16x32_bf16 v[106:109], v[6:9], v[46:49], v[106:109]
	v_mfma_f32_16x16x32_bf16 v[102:105], v[10:13], v[46:49], v[102:105]
	v_mfma_f32_16x16x32_bf16 v[98:101], v[14:17], v[46:49], v[98:101]
	ds_read_b128 v[46:49], v178 offset:0x3800
	s_waitcnt lgkmcnt(2)
	s_nop 0
	v_mfma_f32_16x16x32_bf16 v[158:161], v[2:5], v[130:133], v[94:97]
	v_mfma_f32_16x16x32_bf16 v[162:165], v[6:9], v[130:133], v[90:93]
	v_mfma_f32_16x16x32_bf16 v[166:169], v[10:13], v[130:133], v[86:89]
	v_mfma_f32_16x16x32_bf16 v[130:133], v[14:17], v[130:133], v[82:85]
	s_waitcnt lgkmcnt(1)
	s_nop 0
	v_mfma_f32_16x16x32_bf16 v[66:69], v[14:17], v[114:117], v[66:69]
	v_mfma_f32_16x16x32_bf16 v[170:173], v[2:5], v[114:117], v[78:81]
	v_mfma_f32_16x16x32_bf16 v[174:177], v[6:9], v[114:117], v[74:77]
	v_mfma_f32_16x16x32_bf16 v[180:183], v[10:13], v[114:117], v[70:73]
	s_waitcnt lgkmcnt(0)
	s_nop 0
	v_mfma_f32_16x16x32_bf16 v[2:5], v[2:5], v[46:49], v[26:29]
	v_mfma_f32_16x16x32_bf16 v[114:117], v[6:9], v[46:49], v[30:33]
	v_mfma_f32_16x16x32_bf16 v[34:37], v[10:13], v[46:49], v[34:37]
	v_mfma_f32_16x16x32_bf16 v[184:187], v[14:17], v[46:49], v[38:41]
	ds_read_b128 v[188:191], v196 offset:0x400
	ds_read_b128 v[192:195], v196 offset:0xc00
	ds_read_b128 v[202:205], v196 offset:0x1400
	ds_read_b128 v[206:209], v196 offset:0x1c00
	ds_read_b128 v[6:9], v178 offset:0x400
	ds_read_b128 v[10:13], v178 offset:0xc00
	ds_read_b128 v[14:17], v178 offset:0x1400
	s_nop 0
	s_waitcnt lgkmcnt(2)
	s_nop 0
	v_mfma_f32_16x16x32_bf16 v[94:97], v[192:195], v[6:9], v[58:61]
	v_mfma_f32_16x16x32_bf16 v[62:65], v[202:205], v[6:9], v[62:65]
	v_mfma_f32_16x16x32_bf16 v[30:33], v[206:209], v[6:9], v[18:21]
	v_mfma_f32_16x16x32_bf16 v[210:213], v[188:191], v[6:9], v[54:57]
	ds_read_b128 v[6:9], v178 offset:0x1c00
	s_waitcnt lgkmcnt(2)
	s_nop 0
	v_mfma_f32_16x16x32_bf16 v[90:93], v[192:195], v[10:13], v[154:157]
	v_mfma_f32_16x16x32_bf16 v[58:61], v[202:205], v[10:13], v[150:153]
	v_mfma_f32_16x16x32_bf16 v[26:29], v[206:209], v[10:13], v[22:25]
	v_mfma_f32_16x16x32_bf16 v[146:149], v[188:191], v[10:13], v[146:149]
	ds_read_b128 v[10:13], v178 offset:0x2400
	s_waitcnt lgkmcnt(2)
	s_nop 0
	v_mfma_f32_16x16x32_bf16 v[86:89], v[192:195], v[14:17], v[138:141]
	v_mfma_f32_16x16x32_bf16 v[54:57], v[202:205], v[14:17], v[134:137]
	v_mfma_f32_16x16x32_bf16 v[22:25], v[206:209], v[14:17], v[50:53]
	v_mfma_f32_16x16x32_bf16 v[142:145], v[188:191], v[14:17], v[142:145]
	ds_read_b128 v[38:41], v178 offset:0x2c00
	s_waitcnt lgkmcnt(2)
	s_nop 0
	v_mfma_f32_16x16x32_bf16 v[126:129], v[188:191], v[6:9], v[126:129]
	v_mfma_f32_16x16x32_bf16 v[82:85], v[192:195], v[6:9], v[122:125]
	v_mfma_f32_16x16x32_bf16 v[50:53], v[202:205], v[6:9], v[118:121]
	v_mfma_f32_16x16x32_bf16 v[18:21], v[206:209], v[6:9], v[42:45]
	ds_read_b128 v[6:9], v178 offset:0x3400
	s_waitcnt lgkmcnt(2)
	s_nop 0
	v_mfma_f32_16x16x32_bf16 v[110:113], v[188:191], v[10:13], v[110:113]
	v_mfma_f32_16x16x32_bf16 v[78:81], v[192:195], v[10:13], v[106:109]
	v_mfma_f32_16x16x32_bf16 v[46:49], v[202:205], v[10:13], v[102:105]
	v_mfma_f32_16x16x32_bf16 v[14:17], v[206:209], v[10:13], v[98:101]
	ds_read_b128 v[98:101], v178 offset:0x3c00
	s_waitcnt lgkmcnt(2)
	s_nop 0
	v_mfma_f32_16x16x32_bf16 v[106:109], v[188:191], v[38:41], v[158:161]
	v_mfma_f32_16x16x32_bf16 v[74:77], v[192:195], v[38:41], v[162:165]
	v_mfma_f32_16x16x32_bf16 v[42:45], v[202:205], v[38:41], v[166:169]
	v_mfma_f32_16x16x32_bf16 v[10:13], v[206:209], v[38:41], v[130:133]
	s_waitcnt lgkmcnt(1)
	s_nop 0
	v_mfma_f32_16x16x32_bf16 v[118:121], v[188:191], v[6:9], v[170:173]
	v_mfma_f32_16x16x32_bf16 v[70:73], v[192:195], v[6:9], v[174:177]
	v_mfma_f32_16x16x32_bf16 v[38:41], v[202:205], v[6:9], v[180:183]
	v_mfma_f32_16x16x32_bf16 v[6:9], v[206:209], v[6:9], v[66:69]
	s_waitcnt lgkmcnt(0)
	s_nop 0
	v_mfma_f32_16x16x32_bf16 v[122:125], v[188:191], v[98:101], v[2:5]
	v_mfma_f32_16x16x32_bf16 v[66:69], v[192:195], v[98:101], v[114:117]
	v_mfma_f32_16x16x32_bf16 v[34:37], v[202:205], v[98:101], v[34:37]
	v_mfma_f32_16x16x32_bf16 v[2:5], v[206:209], v[98:101], v[184:187]
	v_lshrrev_b32_e32 v98, 2, v199
	v_and_b32_e32 v98, 12, v98
	v_lshl_or_b32 v104, v200, 6, v98
	v_lshlrev_b32_e32 v105, 2, v104
	s_waitcnt lgkmcnt(0)
	s_barrier
	global_load_dwordx4 v[114:117], v105, s[6:7]
	v_lshrrev_b32_e32 v98, 1, v199
	v_lshlrev_b32_e32 v99, 16, v198
	v_lshlrev_b32_e32 v100, 9, v179
	v_and_b32_e32 v102, 8, v98
	v_lshrrev_b32_e32 v98, 3, v104
	v_add3_u32 v103, 0, v99, v100
	v_xor_b32_e32 v130, v98, v179
	v_bitop3_b32 v131, v98, v179, 16 bitop3:0x1e
	global_load_dwordx4 v[98:101], v105, s[6:7] offset:64
	v_lshlrev_b32_e32 v130, 4, v130
	v_lshlrev_b32_e32 v131, 4, v131
	v_add3_u32 v130, v103, v130, v102
	v_add3_u32 v131, v103, v131, v102
	s_movk_i32 s0, 0x200
	s_waitcnt vmcnt(1)
	v_add_f32_e32 v132, v210, v114
	v_add_f32_e32 v133, v211, v115
	v_add_f32_e32 v134, v212, v116
	v_add_f32_e32 v135, v213, v117
	v_add_f32_e32 v140, v142, v114
	v_add_f32_e32 v141, v143, v115
	v_add_f32_e32 v142, v144, v116
	v_add_f32_e32 v143, v145, v117
	v_add_f32_e32 v110, v110, v114
	v_add_f32_e32 v111, v111, v115
	v_add_f32_e32 v106, v106, v114
	v_add_f32_e32 v107, v107, v115
	v_add_f32_e32 v136, v146, v114
	v_add_f32_e32 v137, v147, v115
	v_add_f32_e32 v138, v148, v116
	v_add_f32_e32 v139, v149, v117
	v_add_f32_e32 v126, v126, v114
	v_add_f32_e32 v127, v127, v115
	v_add_f32_e32 v128, v128, v116
	v_add_f32_e32 v129, v129, v117
	v_add_f32_e32 v112, v112, v116
	v_add_f32_e32 v113, v113, v117
	v_add_f32_e32 v108, v108, v116
	v_add_f32_e32 v109, v109, v117
	v_max_f32_e32 v132, 0, v132
	v_max_f32_e32 v133, 0, v133
	v_max_f32_e32 v134, 0, v134
	v_max_f32_e32 v135, 0, v135
	v_max_f32_e32 v140, 0, v140
	v_max_f32_e32 v141, 0, v141
	v_max_f32_e32 v142, 0, v142
	v_max_f32_e32 v143, 0, v143
	v_max_f32_e32 v144, 0, v110
	v_max_f32_e32 v145, 0, v111
	v_max_f32_e32 v148, 0, v106
	v_max_f32_e32 v149, 0, v107
	v_cvt_pk_bf16_f32 v106, v132, v133
	v_cvt_pk_bf16_f32 v107, v134, v135
	v_cvt_pk_bf16_f32 v110, v140, v141
	v_cvt_pk_bf16_f32 v111, v142, v143
	v_add_f32_e32 v118, v118, v114
	v_add_f32_e32 v119, v119, v115
	v_max_f32_e32 v136, 0, v136
	v_max_f32_e32 v137, 0, v137
	v_max_f32_e32 v138, 0, v138
	v_max_f32_e32 v139, 0, v139
	v_max_f32_e32 v126, 0, v126
	v_max_f32_e32 v127, 0, v127
	v_max_f32_e32 v128, 0, v128
	v_max_f32_e32 v129, 0, v129
	v_max_f32_e32 v146, 0, v112
	v_max_f32_e32 v147, 0, v113
	v_max_f32_e32 v150, 0, v108
	v_max_f32_e32 v151, 0, v109
	v_cvt_pk_bf16_f32 v108, v136, v137
	v_cvt_pk_bf16_f32 v109, v138, v139
	v_cvt_pk_bf16_f32 v112, v126, v127
	v_cvt_pk_bf16_f32 v113, v128, v129
	ds_write2st64_b64 v130, v[106:107], v[110:111] offset1:32
	ds_write2st64_b64 v131, v[108:109], v[112:113] offset0:16 offset1:48
	v_add_f32_e32 v106, v121, v117
	v_add_f32_e32 v120, v120, v116
	v_max_f32_e32 v152, 0, v118
	v_max_f32_e32 v153, 0, v119
	v_max_f32_e32 v107, 0, v106
	v_cvt_pk_bf16_f32 v106, v152, v153
	v_max_f32_e32 v120, 0, v120
	v_cvt_pk_bf16_f32 v118, v144, v145
	v_cvt_pk_bf16_f32 v119, v146, v147
	v_cvt_pk_bf16_f32 v107, v120, v107
	ds_write2st64_b64 v130, v[118:119], v[106:107] offset0:64 offset1:96
	v_add_f32_e32 v106, v122, v114
	v_max_f32_e32 v106, 0, v106
	v_add_f32_e32 v107, v123, v115
	v_max_f32_e32 v107, 0, v107
	v_add_f32_e32 v108, v124, v116
	v_add_f32_e32 v109, v125, v117
	v_cvt_pk_bf16_f32 v106, v106, v107
	v_cvt_pk_bf16_f32 v126, v148, v149
	v_cvt_pk_bf16_f32 v127, v150, v151
	v_max_f32_e32 v108, 0, v108
	v_max_f32_e32 v109, 0, v109
	v_cvt_pk_bf16_f32 v107, v108, v109
	ds_write2st64_b64 v131, v[126:127], v[106:107] offset0:80 offset1:112
	v_or_b32_e32 v106, 16, v104
	s_waitcnt vmcnt(0)
	v_add_f32_e32 v94, v94, v98
	v_add_f32_e32 v95, v95, v99
	v_add_f32_e32 v96, v96, v100
	v_lshrrev_b32_e32 v106, 3, v106
	v_max_f32_e32 v94, 0, v94
	v_max_f32_e32 v95, 0, v95
	v_max_f32_e32 v96, 0, v96
	v_add_f32_e32 v97, v97, v101
	v_max_f32_e32 v97, 0, v97
	v_cvt_pk_bf16_f32 v94, v94, v95
	v_cvt_pk_bf16_f32 v95, v96, v97
	v_xor_b32_e32 v96, v106, v179
	v_lshlrev_b32_e32 v96, 4, v96
	v_add3_u32 v107, v103, v96, v102
	v_add_f32_e32 v90, v90, v98
	v_add_f32_e32 v91, v91, v99
	v_add_f32_e32 v92, v92, v100
	ds_write_b64 v107, v[94:95]
	v_max_f32_e32 v90, 0, v90
	v_max_f32_e32 v91, 0, v91
	global_load_dwordx4 v[94:97], v105, s[6:7] offset:128
	v_max_f32_e32 v92, 0, v92
	v_add_f32_e32 v93, v93, v101
	v_max_f32_e32 v93, 0, v93
	v_cvt_pk_bf16_f32 v90, v90, v91
	v_cvt_pk_bf16_f32 v91, v92, v93
	v_bitop3_b32 v92, v106, v179, 16 bitop3:0x1e
	v_add_f32_e32 v66, v66, v98
	v_lshlrev_b32_e32 v92, 4, v92
	v_add_f32_e32 v86, v86, v98
	v_add_f32_e32 v87, v87, v99
	v_add_f32_e32 v82, v82, v98
	v_add_f32_e32 v83, v83, v99
	v_add_f32_e32 v78, v78, v98
	v_add_f32_e32 v79, v79, v99
	v_add_f32_e32 v74, v74, v98
	v_add_f32_e32 v75, v75, v99
	v_add_f32_e32 v70, v70, v98
	v_add_f32_e32 v71, v71, v99
	v_max_f32_e32 v66, 0, v66
	v_add_f32_e32 v67, v67, v99
	v_add3_u32 v92, v103, v92, v102
	v_max_f32_e32 v86, 0, v86
	v_max_f32_e32 v87, 0, v87
	v_add_f32_e32 v88, v88, v100
	v_add_f32_e32 v89, v89, v101
	v_max_f32_e32 v82, 0, v82
	v_max_f32_e32 v83, 0, v83
	v_add_f32_e32 v84, v84, v100
	v_add_f32_e32 v85, v85, v101
	v_max_f32_e32 v78, 0, v78
	v_max_f32_e32 v79, 0, v79
	v_add_f32_e32 v80, v80, v100
	v_add_f32_e32 v81, v81, v101
	v_max_f32_e32 v74, 0, v74
	v_max_f32_e32 v75, 0, v75
	v_add_f32_e32 v76, v76, v100
	v_add_f32_e32 v77, v77, v101
	v_max_f32_e32 v70, 0, v70
	v_max_f32_e32 v71, 0, v71
	v_add_f32_e32 v72, v72, v100
	v_add_f32_e32 v73, v73, v101
	v_max_f32_e32 v67, 0, v67
	v_add_f32_e32 v68, v68, v100
	v_add_f32_e32 v69, v69, v101
	v_cvt_pk_bf16_f32 v66, v66, v67
	ds_write_b64 v92, v[90:91] offset:8192
	v_max_f32_e32 v88, 0, v88
	v_max_f32_e32 v89, 0, v89
	v_cvt_pk_bf16_f32 v86, v86, v87
	v_cvt_pk_bf16_f32 v87, v88, v89
	ds_write_b64 v107, v[86:87] offset:16384
	v_max_f32_e32 v84, 0, v84
	v_max_f32_e32 v85, 0, v85
	v_cvt_pk_bf16_f32 v82, v82, v83
	v_cvt_pk_bf16_f32 v83, v84, v85
	ds_write_b64 v92, v[82:83] offset:24576
	v_max_f32_e32 v80, 0, v80
	v_max_f32_e32 v81, 0, v81
	v_cvt_pk_bf16_f32 v78, v78, v79
	v_cvt_pk_bf16_f32 v79, v80, v81
	ds_write_b64 v107, v[78:79] offset:32768
	v_max_f32_e32 v76, 0, v76
	v_max_f32_e32 v77, 0, v77
	v_cvt_pk_bf16_f32 v74, v74, v75
	v_cvt_pk_bf16_f32 v75, v76, v77
	ds_write_b64 v92, v[74:75] offset:40960
	v_max_f32_e32 v72, 0, v72
	v_max_f32_e32 v73, 0, v73
	v_cvt_pk_bf16_f32 v70, v70, v71
	v_cvt_pk_bf16_f32 v71, v72, v73
	ds_write_b64 v107, v[70:71] offset:49152
	v_max_f32_e32 v68, 0, v68
	v_max_f32_e32 v69, 0, v69
	v_cvt_pk_bf16_f32 v67, v68, v69
	ds_write_b64 v92, v[66:67] offset:57344
	v_or_b32_e32 v66, 32, v104
	v_lshrrev_b32_e32 v70, 3, v66
	global_load_dwordx4 v[66:69], v105, s[6:7] offset:192
	s_waitcnt vmcnt(1)
	v_add_f32_e32 v62, v62, v94
	v_add_f32_e32 v63, v63, v95
	v_add_f32_e32 v64, v64, v96
	v_add_f32_e32 v58, v58, v94
	v_add_f32_e32 v59, v59, v95
	v_add_f32_e32 v60, v60, v96
	v_max_f32_e32 v62, 0, v62
	v_max_f32_e32 v63, 0, v63
	v_max_f32_e32 v64, 0, v64
	v_add_f32_e32 v65, v65, v97
	v_max_f32_e32 v58, 0, v58
	v_max_f32_e32 v59, 0, v59
	v_max_f32_e32 v60, 0, v60
	v_add_f32_e32 v61, v61, v97
	v_max_f32_e32 v65, 0, v65
	v_cvt_pk_bf16_f32 v62, v62, v63
	v_cvt_pk_bf16_f32 v63, v64, v65
	v_xor_b32_e32 v64, v70, v179
	v_max_f32_e32 v61, 0, v61
	v_cvt_pk_bf16_f32 v58, v58, v59
	v_cvt_pk_bf16_f32 v59, v60, v61
	v_bitop3_b32 v60, v70, v179, 16 bitop3:0x1e
	v_add_f32_e32 v34, v34, v94
	v_lshlrev_b32_e32 v64, 4, v64
	v_lshlrev_b32_e32 v60, 4, v60
	v_add_f32_e32 v54, v54, v94
	v_add_f32_e32 v55, v55, v95
	v_add_f32_e32 v50, v50, v94
	v_add_f32_e32 v51, v51, v95
	v_add_f32_e32 v46, v46, v94
	v_add_f32_e32 v47, v47, v95
	v_add_f32_e32 v42, v42, v94
	v_add_f32_e32 v43, v43, v95
	v_add_f32_e32 v38, v38, v94
	v_add_f32_e32 v39, v39, v95
	v_max_f32_e32 v34, 0, v34
	v_add_f32_e32 v35, v35, v95
	v_add3_u32 v64, v103, v64, v102
	v_add3_u32 v60, v103, v60, v102
	v_max_f32_e32 v54, 0, v54
	v_max_f32_e32 v55, 0, v55
	v_add_f32_e32 v56, v56, v96
	v_add_f32_e32 v57, v57, v97
	v_max_f32_e32 v50, 0, v50
	v_max_f32_e32 v51, 0, v51
	v_add_f32_e32 v52, v52, v96
	v_add_f32_e32 v53, v53, v97
	v_max_f32_e32 v46, 0, v46
	v_max_f32_e32 v47, 0, v47
	v_add_f32_e32 v48, v48, v96
	v_add_f32_e32 v49, v49, v97
	v_max_f32_e32 v42, 0, v42
	v_max_f32_e32 v43, 0, v43
	v_add_f32_e32 v44, v44, v96
	v_add_f32_e32 v45, v45, v97
	v_max_f32_e32 v38, 0, v38
	v_max_f32_e32 v39, 0, v39
	v_add_f32_e32 v40, v40, v96
	v_add_f32_e32 v41, v41, v97
	v_max_f32_e32 v35, 0, v35
	v_add_f32_e32 v36, v36, v96
	v_add_f32_e32 v37, v37, v97
	v_cvt_pk_bf16_f32 v34, v34, v35
	ds_write_b64 v64, v[62:63]
	ds_write_b64 v60, v[58:59] offset:8192
	v_max_f32_e32 v56, 0, v56
	v_max_f32_e32 v57, 0, v57
	v_cvt_pk_bf16_f32 v54, v54, v55
	v_cvt_pk_bf16_f32 v55, v56, v57
	ds_write_b64 v64, v[54:55] offset:16384
	v_max_f32_e32 v52, 0, v52
	v_max_f32_e32 v53, 0, v53
	v_cvt_pk_bf16_f32 v50, v50, v51
	v_cvt_pk_bf16_f32 v51, v52, v53
	ds_write_b64 v60, v[50:51] offset:24576
	v_max_f32_e32 v48, 0, v48
	v_max_f32_e32 v49, 0, v49
	v_cvt_pk_bf16_f32 v46, v46, v47
	v_cvt_pk_bf16_f32 v47, v48, v49
	ds_write_b64 v64, v[46:47] offset:32768
	v_max_f32_e32 v44, 0, v44
	v_max_f32_e32 v45, 0, v45
	v_cvt_pk_bf16_f32 v42, v42, v43
	v_cvt_pk_bf16_f32 v43, v44, v45
	ds_write_b64 v60, v[42:43] offset:40960
	v_max_f32_e32 v40, 0, v40
	v_max_f32_e32 v41, 0, v41
	v_cvt_pk_bf16_f32 v38, v38, v39
	v_cvt_pk_bf16_f32 v39, v40, v41
	ds_write_b64 v64, v[38:39] offset:49152
	v_max_f32_e32 v36, 0, v36
	v_max_f32_e32 v37, 0, v37
	v_cvt_pk_bf16_f32 v35, v36, v37
	ds_write_b64 v60, v[34:35] offset:57344
	v_or_b32_e32 v34, 48, v104
	s_waitcnt vmcnt(0)
	v_add_f32_e32 v30, v30, v66
	v_add_f32_e32 v31, v31, v67
	v_add_f32_e32 v32, v32, v68
	v_add_f32_e32 v26, v26, v66
	v_add_f32_e32 v27, v27, v67
	v_add_f32_e32 v28, v28, v68
	v_lshrrev_b32_e32 v34, 3, v34
	v_max_f32_e32 v30, 0, v30
	v_max_f32_e32 v31, 0, v31
	v_max_f32_e32 v32, 0, v32
	v_add_f32_e32 v33, v33, v69
	v_max_f32_e32 v26, 0, v26
	v_max_f32_e32 v27, 0, v27
	v_max_f32_e32 v28, 0, v28
	v_add_f32_e32 v29, v29, v69
	v_max_f32_e32 v33, 0, v33
	v_cvt_pk_bf16_f32 v30, v30, v31
	v_cvt_pk_bf16_f32 v31, v32, v33
	v_xor_b32_e32 v32, v34, v179
	v_max_f32_e32 v29, 0, v29
	v_cvt_pk_bf16_f32 v26, v26, v27
	v_cvt_pk_bf16_f32 v27, v28, v29
	v_bitop3_b32 v28, v34, v179, 16 bitop3:0x1e
	v_add_f32_e32 v2, v2, v66
	v_lshlrev_b32_e32 v32, 4, v32
	v_lshlrev_b32_e32 v28, 4, v28
	v_add_f32_e32 v22, v22, v66
	v_add_f32_e32 v23, v23, v67
	v_add_f32_e32 v18, v18, v66
	v_add_f32_e32 v19, v19, v67
	v_add_f32_e32 v14, v14, v66
	v_add_f32_e32 v15, v15, v67
	v_add_f32_e32 v10, v10, v66
	v_add_f32_e32 v11, v11, v67
	v_add_f32_e32 v6, v6, v66
	v_add_f32_e32 v7, v7, v67
	v_max_f32_e32 v2, 0, v2
	v_add_f32_e32 v3, v3, v67
	v_add3_u32 v32, v103, v32, v102
	v_add3_u32 v28, v103, v28, v102
	v_max_f32_e32 v22, 0, v22
	v_max_f32_e32 v23, 0, v23
	v_add_f32_e32 v24, v24, v68
	v_add_f32_e32 v25, v25, v69
	v_max_f32_e32 v18, 0, v18
	v_max_f32_e32 v19, 0, v19
	v_add_f32_e32 v20, v20, v68
	v_add_f32_e32 v21, v21, v69
	v_max_f32_e32 v14, 0, v14
	v_max_f32_e32 v15, 0, v15
	v_add_f32_e32 v16, v16, v68
	v_add_f32_e32 v17, v17, v69
	v_max_f32_e32 v10, 0, v10
	v_max_f32_e32 v11, 0, v11
	v_add_f32_e32 v12, v12, v68
	v_add_f32_e32 v13, v13, v69
	v_max_f32_e32 v6, 0, v6
	v_max_f32_e32 v7, 0, v7
	v_add_f32_e32 v8, v8, v68
	v_add_f32_e32 v9, v9, v69
	v_max_f32_e32 v3, 0, v3
	v_add_f32_e32 v4, v4, v68
	v_add_f32_e32 v5, v5, v69
	v_cvt_pk_bf16_f32 v2, v2, v3
	ds_write_b64 v32, v[30:31]
	ds_write_b64 v28, v[26:27] offset:8192
	v_max_f32_e32 v24, 0, v24
	v_max_f32_e32 v25, 0, v25
	v_cvt_pk_bf16_f32 v22, v22, v23
	v_cvt_pk_bf16_f32 v23, v24, v25
	ds_write_b64 v32, v[22:23] offset:16384
	v_max_f32_e32 v20, 0, v20
	v_max_f32_e32 v21, 0, v21
	v_cvt_pk_bf16_f32 v18, v18, v19
	v_cvt_pk_bf16_f32 v19, v20, v21
	ds_write_b64 v28, v[18:19] offset:24576
	v_max_f32_e32 v16, 0, v16
	v_max_f32_e32 v17, 0, v17
	v_cvt_pk_bf16_f32 v14, v14, v15
	v_cvt_pk_bf16_f32 v15, v16, v17
	ds_write_b64 v32, v[14:15] offset:32768
	v_max_f32_e32 v12, 0, v12
	v_max_f32_e32 v13, 0, v13
	v_cvt_pk_bf16_f32 v10, v10, v11
	v_cvt_pk_bf16_f32 v11, v12, v13
	ds_write_b64 v28, v[10:11] offset:40960
	v_max_f32_e32 v8, 0, v8
	v_max_f32_e32 v9, 0, v9
	v_cvt_pk_bf16_f32 v6, v6, v7
	v_cvt_pk_bf16_f32 v7, v8, v9
	ds_write_b64 v32, v[6:7] offset:49152
	v_max_f32_e32 v4, 0, v4
	v_max_f32_e32 v5, 0, v5
	v_cvt_pk_bf16_f32 v3, v4, v5
	ds_write_b64 v28, v[2:3] offset:57344
	v_and_b32_e32 v2, 0x1f0, v1
	v_lshrrev_b32_e32 v1, 5, v0
	v_xor_b32_e32 v4, v1, v0
	v_mov_b32_e32 v3, 0
	v_lshlrev_b32_e32 v4, 4, v4
	v_lshl_add_u64 v[12:13], s[4:5], 0, v[2:3]
	v_lshlrev_b32_e32 v2, 9, v1
	v_and_b32_e32 v16, 0x1f0, v4
	v_add3_u32 v2, 0, v2, v16
	s_waitcnt lgkmcnt(0)
	s_barrier
	ds_read_b128 v[4:7], v2
	v_lshlrev_b32_e32 v2, 11, v1
	v_lshl_add_u64 v[14:15], v[12:13], 0, v[2:3]
	v_or_b32_e32 v2, 0x200, v0
	v_lshrrev_b32_e32 v2, 5, v2
	v_xor_b32_e32 v9, v2, v0
	v_lshlrev_b32_e32 v9, 4, v9
	v_lshlrev_b32_e32 v8, 9, v2
	v_and_b32_e32 v9, 0x1f0, v9
	v_add3_u32 v8, 0, v8, v9
	ds_read_b128 v[8:11], v8
	v_lshlrev_b32_e32 v2, 11, v2
	s_waitcnt lgkmcnt(1)
	global_store_dwordx4 v[14:15], v[4:7], off
	s_nop 1
	v_lshl_add_u64 v[4:5], v[12:13], 0, v[2:3]
	s_waitcnt lgkmcnt(0)
	global_store_dwordx4 v[4:5], v[8:11], off
	v_or_b32_e32 v2, 32, v1
	v_lshlrev_b32_e32 v4, 9, v2
	v_or_b32_e32 v8, 0x600, v0
	v_lshrrev_b32_e32 v17, 5, v8
	v_xor_b32_e32 v9, v17, v0
	v_lshlrev_b32_e32 v9, 4, v9
	v_add3_u32 v4, 0, v4, v16
	v_lshlrev_b32_e32 v8, 9, v17
	v_and_b32_e32 v9, 0x1f0, v9
	ds_read_b128 v[4:7], v4
	v_add3_u32 v8, 0, v8, v9
	ds_read_b128 v[8:11], v8
	v_lshlrev_b32_e32 v2, 11, v2
	v_lshl_add_u64 v[14:15], v[12:13], 0, v[2:3]
	v_lshlrev_b32_e32 v2, 11, v17
	s_waitcnt lgkmcnt(1)
	global_store_dwordx4 v[14:15], v[4:7], off
	s_nop 1
	v_lshl_add_u64 v[4:5], v[12:13], 0, v[2:3]
	s_waitcnt lgkmcnt(0)
	global_store_dwordx4 v[4:5], v[8:11], off
	v_or_b32_e32 v2, 64, v1
	v_lshlrev_b32_e32 v4, 9, v2
	v_or_b32_e32 v8, 0xa00, v0
	v_lshrrev_b32_e32 v17, 5, v8
	v_xor_b32_e32 v9, v17, v0
	v_lshlrev_b32_e32 v9, 4, v9
	v_add3_u32 v4, 0, v4, v16
	v_lshlrev_b32_e32 v8, 9, v17
	v_and_b32_e32 v9, 0x1f0, v9
	ds_read_b128 v[4:7], v4
	v_add3_u32 v8, 0, v8, v9
	ds_read_b128 v[8:11], v8
	v_lshlrev_b32_e32 v2, 11, v2
	v_lshl_add_u64 v[14:15], v[12:13], 0, v[2:3]
	v_lshlrev_b32_e32 v2, 11, v17
	s_waitcnt lgkmcnt(1)
	global_store_dwordx4 v[14:15], v[4:7], off
	s_nop 1
	v_lshl_add_u64 v[4:5], v[12:13], 0, v[2:3]
	s_waitcnt lgkmcnt(0)
	global_store_dwordx4 v[4:5], v[8:11], off
	v_or_b32_e32 v2, 0x60, v1
	v_lshlrev_b32_e32 v4, 9, v2
	v_or_b32_e32 v8, 0xe00, v0
	v_lshrrev_b32_e32 v17, 5, v8
	v_xor_b32_e32 v9, v17, v0
	v_lshlrev_b32_e32 v9, 4, v9
	v_add3_u32 v4, 0, v4, v16
	v_lshlrev_b32_e32 v8, 9, v17
	v_and_b32_e32 v9, 0x1f0, v9
	ds_read_b128 v[4:7], v4
	v_add3_u32 v8, 0, v8, v9
	ds_read_b128 v[8:11], v8
	v_lshlrev_b32_e32 v2, 11, v2
	v_lshl_add_u64 v[14:15], v[12:13], 0, v[2:3]
	v_lshlrev_b32_e32 v2, 11, v17
	s_waitcnt lgkmcnt(1)
	global_store_dwordx4 v[14:15], v[4:7], off
	s_nop 1
	v_lshl_add_u64 v[4:5], v[12:13], 0, v[2:3]
	s_waitcnt lgkmcnt(0)
	global_store_dwordx4 v[4:5], v[8:11], off
	v_or_b32_e32 v2, 0x80, v1
	v_lshlrev_b32_e32 v4, 9, v2
	v_or_b32_e32 v8, 0x1200, v0
	v_lshrrev_b32_e32 v17, 5, v8
	v_xor_b32_e32 v9, v17, v0
	v_lshlrev_b32_e32 v9, 4, v9
	v_add3_u32 v4, 0, v4, v16
	v_lshlrev_b32_e32 v8, 9, v17
	v_and_b32_e32 v9, 0x1f0, v9
	ds_read_b128 v[4:7], v4
	v_add3_u32 v8, 0, v8, v9
	ds_read_b128 v[8:11], v8
	v_lshlrev_b32_e32 v2, 11, v2
	v_lshl_add_u64 v[14:15], v[12:13], 0, v[2:3]
	v_lshlrev_b32_e32 v2, 11, v17
	s_waitcnt lgkmcnt(1)
	global_store_dwordx4 v[14:15], v[4:7], off
	s_nop 1
	v_lshl_add_u64 v[4:5], v[12:13], 0, v[2:3]
	s_waitcnt lgkmcnt(0)
	global_store_dwordx4 v[4:5], v[8:11], off
	v_or_b32_e32 v2, 0xa0, v1
	v_lshlrev_b32_e32 v4, 9, v2
	v_or_b32_e32 v8, 0x1600, v0
	v_lshrrev_b32_e32 v17, 5, v8
	v_xor_b32_e32 v9, v17, v0
	v_lshlrev_b32_e32 v9, 4, v9
	v_add3_u32 v4, 0, v4, v16
	v_lshlrev_b32_e32 v8, 9, v17
	v_and_b32_e32 v9, 0x1f0, v9
	ds_read_b128 v[4:7], v4
	v_add3_u32 v8, 0, v8, v9
	ds_read_b128 v[8:11], v8
	v_lshlrev_b32_e32 v2, 11, v2
	v_lshl_add_u64 v[14:15], v[12:13], 0, v[2:3]
	v_lshlrev_b32_e32 v2, 11, v17
	s_waitcnt lgkmcnt(1)
	global_store_dwordx4 v[14:15], v[4:7], off
	s_nop 1
	v_lshl_add_u64 v[4:5], v[12:13], 0, v[2:3]
	s_waitcnt lgkmcnt(0)
	global_store_dwordx4 v[4:5], v[8:11], off
	v_or_b32_e32 v2, 0xc0, v1
	v_lshlrev_b32_e32 v4, 9, v2
	v_or_b32_e32 v8, 0x1a00, v0
	v_lshrrev_b32_e32 v17, 5, v8
	v_xor_b32_e32 v9, v17, v0
	v_add3_u32 v4, 0, v4, v16
	v_lshlrev_b32_e32 v9, 4, v9
	ds_read_b128 v[4:7], v4
	v_lshlrev_b32_e32 v8, 9, v17
	v_and_b32_e32 v9, 0x1f0, v9
	v_add3_u32 v8, 0, v8, v9
	ds_read_b128 v[8:11], v8
	v_lshlrev_b32_e32 v2, 11, v2
	v_lshl_add_u64 v[14:15], v[12:13], 0, v[2:3]
	v_lshlrev_b32_e32 v2, 11, v17
	v_or_b32_e32 v1, 0xe0, v1
	s_waitcnt lgkmcnt(1)
	global_store_dwordx4 v[14:15], v[4:7], off
	s_nop 1
	v_lshl_add_u64 v[4:5], v[12:13], 0, v[2:3]
	v_lshlrev_b32_e32 v2, 9, v1
	v_add3_u32 v2, 0, v2, v16
	s_waitcnt lgkmcnt(0)
	global_store_dwordx4 v[4:5], v[8:11], off
	ds_read_b128 v[4:7], v2
	v_lshlrev_b32_e32 v2, 11, v1
	v_or_b32_e32 v1, 0x1e00, v0
	v_lshrrev_b32_e32 v1, 5, v1
	v_xor_b32_e32 v9, v1, v0
	v_lshlrev_b32_e32 v9, 4, v9
	v_lshlrev_b32_e32 v8, 9, v1
	v_and_b32_e32 v9, 0x1f0, v9
	v_add3_u32 v8, 0, v8, v9
	ds_read_b128 v[8:11], v8
	v_lshl_add_u64 v[14:15], v[12:13], 0, v[2:3]
	v_lshlrev_b32_e32 v2, 11, v1
	s_waitcnt lgkmcnt(1)
	global_store_dwordx4 v[14:15], v[4:7], off
	s_nop 1
	v_lshl_add_u64 v[4:5], v[12:13], 0, v[2:3]
	s_waitcnt lgkmcnt(0)
	global_store_dwordx4 v[4:5], v[8:11], off
	s_waitcnt lgkmcnt(0)
	s_barrier
	s_lshl_b32 s3, s2, 3
	s_and_b32 s3, s3, 56
	s_ashr_i32 s17, s2, 5
	s_add_i32 s20, s3, s17
	s_ashr_i32 s21, s20, 31
	s_bfe_u32 s16, s2, 0x20003
	s_lshl_b64 s[4:5], s[20:21], 17
	s_lshl_b64 s[6:7], s[20:21], 19
	s_add_u32 s6, s12, s6
	s_addc_u32 s7, s13, s7
	s_lshl_b32 s3, s16, 19
	s_add_u32 s3, s14, s3
	v_ashrrev_i32_e32 v2, 6, v0
	v_lshlrev_b32_e32 v1, 4, v0
	s_addc_u32 s13, s15, 0
	v_lshlrev_b32_e32 v4, 9, v2
	v_and_b32_e32 v5, 0x1f0, v1
	s_add_u32 s12, s3, 0x400000
	v_and_or_b32 v32, v4, s0, v5
	v_lshlrev_b32_e32 v4, 5, v2
	v_and_b32_e32 v5, 48, v1
	s_addc_u32 s13, s13, 0
	v_bitop3_b32 v4, v4, v5, 32 bitop3:0x6c
	s_and_b32 s15, s2, 8
	s_add_i32 s3, s20, 3
	v_bfe_u32 v31, v0, 5, 1
	v_lshrrev_b32_e32 v34, 1, v4
	v_add_u32_e32 v4, s15, v2
	s_mov_b32 s20, 0x3ffffe
	v_and_or_b32 v30, v4, s20, v31
	v_bfe_i32 v5, v30, 0, 22
	v_bfe_u32 v4, v30, 21, 1
	v_add_u32_e32 v6, v5, v4
	v_lshlrev_b32_e32 v4, 3, v6
	v_and_b32_e32 v6, 0x7fffffe, v6
	s_lshl_b32 s0, s17, 4
	v_sub_u32_e32 v5, v5, v6
	s_and_b32 s17, s0, 16
	v_lshl_or_b32 v6, v5, 5, v34
	v_add_u32_e32 v5, s17, v2
	v_and_or_b32 v35, v5, s20, v31
	v_bfe_i32 v7, v35, 0, 22
	v_bfe_u32 v8, v35, 21, 1
	v_add_u32_e32 v8, v7, v8
	v_lshlrev_b32_e32 v9, 3, v8
	v_and_b32_e32 v8, 0x7fffffe, v8
	v_add_u32_e32 v5, 8, v5
	v_sub_u32_e32 v7, v7, v8
	v_and_or_b32 v36, v5, s20, v31
	v_lshl_or_b32 v98, v7, 5, v34
	v_bfe_i32 v5, v36, 0, 22
	v_bfe_u32 v7, v36, 21, 1
	v_add_u32_e32 v7, v5, v7
	v_lshrrev_b32_e32 v33, 6, v32
	v_lshlrev_b32_e32 v8, 3, v7
	v_and_b32_e32 v7, 0x7fffffe, v7
	s_and_b32 s3, s3, 15
	v_and_or_b32 v4, v4, -16, v33
	v_sub_u32_e32 v5, v5, v7
	v_and_or_b32 v14, v9, -16, v33
	v_lshl_or_b32 v100, v5, 5, v34
	v_ashrrev_i32_e32 v5, 31, v4
	s_lshl_b32 s14, s3, 6
	s_lshl_b32 s0, s3, 8
	s_lshl_b32 s2, s3, 7
	v_and_or_b32 v16, v8, -16, v33
	v_lshlrev_b64 v[4:5], 12, v[4:5]
	s_add_u32 s2, s12, s2
	v_ashrrev_i32_e32 v15, 31, v14
	v_lshl_add_u64 v[4:5], s[6:7], 0, v[4:5]
	v_ashrrev_i32_e32 v7, 31, v6
	s_addc_u32 s3, s13, 0
	v_lshlrev_b64 v[102:103], 11, v[14:15]
	v_ashrrev_i32_e32 v99, 31, v98
	v_ashrrev_i32_e32 v17, 31, v16
	v_lshl_add_u64 v[8:9], v[4:5], 0, s[0:1]
	v_lshlrev_b64 v[38:39], 2, v[6:7]
	v_lshl_add_u64 v[14:15], s[2:3], 0, v[102:103]
	v_lshlrev_b64 v[22:23], 1, v[98:99]
	v_lshlrev_b64 v[104:105], 11, v[16:17]
	v_ashrrev_i32_e32 v101, 31, v100
	v_lshl_add_u64 v[18:19], v[8:9], 0, v[38:39]
	v_lshl_add_u64 v[24:25], v[14:15], 0, v[22:23]
	v_lshl_add_u64 v[14:15], s[2:3], 0, v[104:105]
	v_lshlrev_b64 v[26:27], 1, v[100:101]
	global_load_dwordx4 v[6:9], v[18:19], off offset:16
	global_load_dwordx4 v[10:13], v[18:19], off
	v_lshl_add_u64 v[28:29], v[14:15], 0, v[26:27]
	global_load_dwordx4 v[14:17], v[24:25], off
	global_load_dwordx4 v[18:21], v[28:29], off
	v_lshlrev_b32_e32 v24, 10, v30
	v_or_b32_e32 v125, v24, v32
	v_xad_u32 v24, s15, 8, v2
	v_and_or_b32 v24, v24, s20, v31
	v_lshlrev_b32_e32 v25, 10, v24
	v_or_b32_e32 v122, v25, v32
	v_bfe_i32 v25, v24, 0, 22
	v_bfe_u32 v24, v24, 21, 1
	v_add_u32_e32 v28, v25, v24
	v_lshlrev_b32_e32 v24, 3, v28
	v_and_b32_e32 v28, 0x7fffffe, v28
	v_sub_u32_e32 v25, v25, v28
	v_lshl_or_b32 v28, v25, 5, v34
	v_lshlrev_b32_e32 v25, 10, v35
	v_or_b32_e32 v126, v25, v32
	v_lshlrev_b32_e32 v25, 10, v36
	v_or_b32_e32 v127, v25, v32
	v_xad_u32 v25, s17, 16, v2
	v_and_or_b32 v25, v25, s20, v31
	v_lshlrev_b32_e32 v29, 10, v25
	v_or_b32_e32 v123, v29, v32
	v_bfe_i32 v29, v25, 0, 22
	v_bfe_u32 v25, v25, 21, 1
	v_add_u32_e32 v25, v29, v25
	v_and_b32_e32 v121, 3, v2
	v_lshlrev_b32_e32 v30, 3, v25
	v_and_b32_e32 v25, 0x7fffffe, v25
	v_xad_u32 v2, s17, 24, v2
	v_sub_u32_e32 v25, v29, v25
	v_and_or_b32 v2, v2, s20, v31
	v_lshl_or_b32 v106, v25, 5, v34
	v_lshlrev_b32_e32 v25, 10, v2
	v_or_b32_e32 v124, v25, v32
	v_bfe_i32 v25, v2, 0, 22
	v_bfe_u32 v2, v2, 21, 1
	v_add_u32_e32 v2, v25, v2
	v_lshlrev_b32_e32 v29, 3, v2
	v_and_b32_e32 v2, 0x7fffffe, v2
	v_and_b32_e32 v118, 15, v0
	v_sub_u32_e32 v2, v25, v2
	v_lshlrev_b32_e32 v25, 2, v0
	v_ashrrev_i32_e32 v120, 8, v0
	v_and_or_b32 v32, v29, -16, v33
	v_lshl_or_b32 v108, v2, 5, v34
	v_and_b32_e32 v2, 48, v0
	v_and_b32_e32 v25, 32, v25
	v_lshlrev_b32_e32 v29, 6, v118
	v_and_b32_e32 v119, 63, v0
	v_and_or_b32 v24, v24, -16, v33
	v_and_or_b32 v30, v30, -16, v33
	v_lshlrev_b32_e32 v68, 13, v120
	v_bitop3_b32 v2, v29, v25, v2 bitop3:0x36
	v_ashrrev_i32_e32 v25, 31, v24
	v_lshlrev_b64 v[24:25], 12, v[24:25]
	v_lshl_add_u64 v[56:57], s[6:7], 0, v[24:25]
	v_ashrrev_i32_e32 v29, 31, v28
	v_lshl_add_u64 v[24:25], v[56:57], 0, s[0:1]
	v_lshlrev_b64 v[58:59], 2, v[28:29]
	v_ashrrev_i32_e32 v31, 31, v30
	v_lshl_add_u64 v[24:25], v[24:25], 0, v[58:59]
	v_lshlrev_b64 v[110:111], 11, v[30:31]
	v_ashrrev_i32_e32 v107, 31, v106
	v_ashrrev_i32_e32 v33, 31, v32
	global_load_dwordx4 v[40:43], v[24:25], off offset:16
	global_load_dwordx4 v[44:47], v[24:25], off
	v_lshl_add_u64 v[24:25], s[2:3], 0, v[110:111]
	v_lshlrev_b64 v[60:61], 1, v[106:107]
	v_lshlrev_b64 v[112:113], 11, v[32:33]
	v_ashrrev_i32_e32 v109, 31, v108
	v_lshl_add_u64 v[24:25], v[24:25], 0, v[60:61]
	v_lshl_add_u64 v[28:29], s[2:3], 0, v[112:113]
	v_lshlrev_b64 v[62:63], 1, v[108:109]
	v_lshl_add_u64 v[28:29], v[28:29], 0, v[62:63]
	global_load_dwordx4 v[48:51], v[24:25], off
	global_load_dwordx4 v[52:55], v[28:29], off
	s_add_i32 s0, s14, 64
	s_and_b32 s2, s0, 0x3c0
	s_lshl_b32 s0, s2, 2
	s_lshl_b32 s2, s2, 1
	v_lshl_add_u64 v[24:25], v[4:5], 0, s[0:1]
	s_add_u32 s2, s12, s2
	v_lshl_add_u64 v[24:25], v[24:25], 0, v[38:39]
	s_addc_u32 s3, s13, 0
	global_load_dwordx4 v[30:33], v[24:25], off offset:16
	global_load_dwordx4 v[34:37], v[24:25], off
	v_lshl_add_u64 v[24:25], s[2:3], 0, v[102:103]
	v_lshl_add_u64 v[64:65], v[24:25], 0, v[22:23]
	v_lshl_add_u64 v[22:23], s[2:3], 0, v[104:105]
	v_lshl_add_u64 v[66:67], v[22:23], 0, v[26:27]
	global_load_dwordx4 v[26:29], v[64:65], off
	global_load_dwordx4 v[22:25], v[66:67], off
	v_add_u32_e32 v64, 0, v125
	s_waitcnt vmcnt(10)
	v_cvt_pk_bf16_f32 v10, v10, v11
	v_cvt_pk_bf16_f32 v11, v12, v13
	v_cvt_pk_bf16_f32 v12, v6, v7
	v_add_u32_e32 v6, 0, v126
	v_cvt_pk_bf16_f32 v13, v8, v9
	ds_write_b128 v64, v[10:13]
	s_waitcnt vmcnt(9)
	ds_write_b128 v6, v[14:17] offset:32768
	v_add_u32_e32 v6, 0, v127
	s_waitcnt vmcnt(8)
	ds_write_b128 v6, v[18:21] offset:32768
	v_add_u32_e32 v10, 0, v122
	s_waitcnt vmcnt(6)
	v_cvt_pk_bf16_f32 v6, v44, v45
	v_cvt_pk_bf16_f32 v7, v46, v47
	v_cvt_pk_bf16_f32 v8, v40, v41
	v_cvt_pk_bf16_f32 v9, v42, v43
	ds_write_b128 v10, v[6:9]
	v_add_u32_e32 v6, 0, v123
	s_waitcnt vmcnt(5)
	ds_write_b128 v6, v[48:51] offset:32768
	v_add_u32_e32 v6, 0, v124
	s_waitcnt vmcnt(4)
	ds_write_b128 v6, v[52:55] offset:32768
	v_lshl_add_u64 v[6:7], v[56:57], 0, s[0:1]
	v_lshl_add_u64 v[14:15], v[6:7], 0, v[58:59]
	global_load_dwordx4 v[6:9], v[14:15], off offset:16
	global_load_dwordx4 v[10:13], v[14:15], off
	v_lshl_add_u64 v[14:15], s[2:3], 0, v[110:111]
	v_lshl_add_u64 v[40:41], v[14:15], 0, v[60:61]
	v_lshl_add_u64 v[14:15], s[2:3], 0, v[112:113]
	v_lshl_add_u64 v[42:43], v[14:15], 0, v[62:63]
	global_load_dwordx4 v[18:21], v[40:41], off
	global_load_dwordx4 v[14:17], v[42:43], off
	v_lshlrev_b32_e32 v40, 13, v121
	s_cmp_lg_u32 0, -1
	s_waitcnt lgkmcnt(0)
	s_cselect_b32 s0, 0, 0
	v_add3_u32 v128, v68, s0, v2
	s_add_i32 s0, s0, 0x8000
	v_add3_u32 v129, v40, s0, v2
	v_lshl_add_u64 v[114:115], v[4:5], 0, v[38:39]
	v_lshl_add_u64 v[116:117], v[56:57], 0, v[58:59]
	s_add_i32 s2, s14, 0x80
	s_mov_b32 s3, 0
	v_mov_b32_e32 v2, v3
	v_mov_b32_e32 v4, v3
	v_mov_b32_e32 v5, v3
	v_mov_b32_e32 v38, v3
	v_mov_b32_e32 v39, v3
	v_mov_b32_e32 v40, v3
	v_mov_b32_e32 v41, v3
	v_mov_b32_e32 v42, v3
	v_mov_b32_e32 v43, v3
	v_mov_b32_e32 v44, v3
	v_mov_b32_e32 v45, v3
	v_mov_b32_e32 v46, v3
	v_mov_b32_e32 v47, v3
	v_mov_b32_e32 v48, v3
	v_mov_b32_e32 v49, v3
	v_mov_b32_e32 v50, v3
	v_mov_b32_e32 v51, v3
	v_mov_b32_e32 v52, v3
	v_mov_b32_e32 v53, v3
	v_mov_b32_e32 v54, v3
	v_mov_b32_e32 v55, v3
	v_mov_b32_e32 v56, v3
	v_mov_b32_e32 v57, v3
	v_mov_b32_e32 v58, v3
	v_mov_b32_e32 v59, v3
	v_mov_b32_e32 v60, v3
	v_mov_b32_e32 v61, v3
	v_mov_b32_e32 v62, v3
	v_mov_b32_e32 v63, v3
	v_mov_b32_e32 v64, v3
	v_mov_b32_e32 v65, v3
	v_mov_b32_e32 v66, v3
	v_mov_b32_e32 v67, v3
	v_mov_b32_e32 v68, v3
	v_mov_b32_e32 v69, v3
	v_mov_b32_e32 v70, v3
	v_mov_b32_e32 v71, v3
	v_mov_b32_e32 v72, v3
	v_mov_b32_e32 v73, v3
	v_mov_b32_e32 v74, v3
	v_mov_b32_e32 v75, v3
	v_mov_b32_e32 v76, v3
	v_mov_b32_e32 v77, v3
	v_mov_b32_e32 v78, v3
	v_mov_b32_e32 v79, v3
	v_mov_b32_e32 v80, v3
	v_mov_b32_e32 v81, v3
	v_mov_b32_e32 v82, v3
	v_mov_b32_e32 v83, v3
	v_mov_b32_e32 v84, v3
	v_mov_b32_e32 v85, v3
	v_mov_b32_e32 v86, v3
	v_mov_b32_e32 v87, v3
	v_mov_b32_e32 v88, v3
	v_mov_b32_e32 v89, v3
	v_mov_b32_e32 v90, v3
	v_mov_b32_e32 v91, v3
	v_mov_b32_e32 v92, v3
	v_mov_b32_e32 v93, v3
	v_mov_b32_e32 v94, v3
	v_mov_b32_e32 v95, v3
	v_mov_b32_e32 v96, v3
	v_mov_b32_e32 v97, v3
	s_and_b32 s0, s3, 0x10000
	v_add_u32_e32 v158, s0, v128
	v_add_u32_e32 v159, s0, v129
	s_barrier
